# baseline (speedup 1.0000x reference)
.Lpp_z2:
	v_xor_b32_e32 v59, 16, v58
	v_lshlrev_b32_e32 v59, 2, v59
	v_xor_b32_e32 v61, 32, v58
	v_lshlrev_b32_e32 v61, 2, v61
	s_mul_i32 s3, s15, 0x900
	v_mul_u32_u24_e32 v57, 0x90, v62
	v_lshl_add_u32 v57, v63, 4, v57
	v_add_u32_e32 v57, s3, v57
	v_mul_u32_u24_e32 v56, 0x480, v62
	v_mul_u32_u24_e32 v55, 0x90, v63
	v_add3_u32 v56, v56, v55, s3
	s_lshl_b32 s6, s15, 1
	v_lshrrev_b32_e32 v55, 2, v63
	v_and_b32_e32 v54, 1, v63
	v_mul_u32_u24_e32 v55, 0xc00, v55
	v_lshl_or_b32 v55, v54, 9, v55
	v_add_u32_e32 v54, s6, v62
	v_lshl_or_b32 v55, v54, 4, v55
	v_mov_b32_e32 v52, 1.0
	s_mul_i32 s6, s8, 0x1800
	s_add_u32 s10, s22, s6
	s_addc_u32 s11, s23, 0
	s_waitcnt vmcnt(1)
	v_pk_mul_f32 v[10:11], v[2:3], v[2:3]
	v_pk_fma_f32 v[10:11], v[4:5], v[4:5], v[10:11]
	s_waitcnt vmcnt(0)
	v_pk_mul_f32 v[12:13], v[6:7], v[6:7]
	v_pk_fma_f32 v[12:13], v[8:9], v[8:9], v[12:13]
	v_add_f32_e32 v10, v10, v11
	v_add_f32_e32 v12, v12, v13
	s_nop 1
	v_add_f32_dpp v10, v10, v10 quad_perm:[1,0,3,2] row_mask:0xf bank_mask:0xf bound_ctrl:1
	v_add_f32_dpp v12, v12, v12 quad_perm:[1,0,3,2] row_mask:0xf bank_mask:0xf bound_ctrl:1
	s_nop 1
	v_add_f32_dpp v10, v10, v10 quad_perm:[2,3,0,1] row_mask:0xf bank_mask:0xf bound_ctrl:1
	v_add_f32_dpp v12, v12, v12 quad_perm:[2,3,0,1] row_mask:0xf bank_mask:0xf bound_ctrl:1
	s_nop 1
	v_add_f32_dpp v10, v10, v10 row_half_mirror row_mask:0xf bank_mask:0xf bound_ctrl:1
	v_add_f32_dpp v12, v12, v12 row_half_mirror row_mask:0xf bank_mask:0xf bound_ctrl:1
	s_nop 1
	v_add_f32_dpp v10, v10, v10 row_mirror row_mask:0xf bank_mask:0xf bound_ctrl:1
	v_add_f32_dpp v12, v12, v12 row_mirror row_mask:0xf bank_mask:0xf bound_ctrl:1
	ds_bpermute_b32 v11, v59, v10
	ds_bpermute_b32 v13, v59, v12
	s_waitcnt lgkmcnt(1)
	v_add_f32_e32 v10, v10, v11
	s_waitcnt lgkmcnt(0)
	v_add_f32_e32 v12, v12, v13
	ds_bpermute_b32 v11, v61, v10
	ds_bpermute_b32 v13, v61, v12
	s_waitcnt lgkmcnt(1)
	v_add_f32_e32 v10, v10, v11
	s_waitcnt lgkmcnt(0)
	v_add_f32_e32 v12, v12, v13
	v_rsq_f32_e32 v10, v10
	v_rsq_f32_e32 v12, v12
	s_nop 0
	v_min_f32_e32 v10, 0x4cbebc20, v10
	v_min_f32_e32 v12, 0x4cbebc20, v12
	v_mul_f32_e32 v10, s14, v10
	v_mul_f32_e32 v12, s14, v12
	v_pk_mul_f32 v[2:3], v[2:3], v[10:11] op_sel_hi:[1,0]
	v_pk_mul_f32 v[4:5], v[4:5], v[10:11] op_sel_hi:[1,0]
	v_pk_mul_f32 v[6:7], v[6:7], v[12:13] op_sel_hi:[1,0]
	v_pk_mul_f32 v[8:9], v[8:9], v[12:13] op_sel_hi:[1,0]
	ds_write_b128 v57, v[2:5]
	ds_write_b128 v57, v[6:9] offset:1152
	s_nop 1
	v_pk_add_f32 v[2:3], v[2:3], v[6:7]
	v_pk_add_f32 v[4:5], v[4:5], v[8:9]
	s_mov_b64 exec, 0xffff
	ds_read_b128 v[12:15], v56
	ds_read_b128 v[16:19], v56 offset:16
	ds_read_b128 v[20:23], v56 offset:32
	ds_read_b128 v[24:27], v56 offset:48
	ds_read_b128 v[28:31], v56 offset:64
	ds_read_b128 v[32:35], v56 offset:80
	ds_read_b128 v[36:39], v56 offset:96
	ds_read_b128 v[40:43], v56 offset:112
	s_waitcnt lgkmcnt(0)
	v_cvt_scalef32_2xpk16_fp6_f32 v[44:49], v[12:27], v[28:43], v52
	s_nop 1
	v_mov_b32_e32 v50, v44
	v_mov_b32_e32 v51, v45
	s_nop 1
	v_mov_b32_dpp v50, v44 row_shl:2 row_mask:0xf bank_mask:0xf
	v_mov_b32_dpp v51, v45 row_shl:2 row_mask:0xf bank_mask:0xf
	s_mov_b64 exec, 0x3333
	global_store_dwordx4 v55, v[44:47], s[10:11]
	global_store_dwordx4 v55, v[48:51], s[10:11] offset:1024
	s_mov_b64 exec, 0xcccc
	global_store_dwordx4 v55, v[46:49], s[10:11] offset:2048
	s_mov_b64 exec, -1
	s_cmp_lt_u32 s8, 0x100
	s_cbranch_scc0 .Lpp_end
	v_add_u32_e32 v10, s3, v60
	ds_write_b128 v10, v[2:5]
	s_waitcnt lgkmcnt(0)
	s_barrier
	s_sub_u32 s6, s15, 8
	s_cmp_gt_u32 s6, 3
	s_cbranch_scc1 .Lpp_end
	s_lshl_b32 s6, s6, 8
	v_lshl_add_u32 v10, v58, 2, s6
	ds_read2st64_b32 v[12:13], v10 offset0:0 offset1:9
	ds_read2st64_b32 v[14:15], v10 offset0:18 offset1:27
	ds_read2st64_b32 v[16:17], v10 offset0:36 offset1:45
	ds_read2st64_b32 v[18:19], v10 offset0:54 offset1:63
	ds_read2st64_b32 v[20:21], v10 offset0:72 offset1:81
	ds_read2st64_b32 v[22:23], v10 offset0:90 offset1:99
	ds_read2st64_b32 v[24:25], v10 offset0:108 offset1:117
	ds_read2st64_b32 v[26:27], v10 offset0:126 offset1:135
	s_cmp_lt_u32 s8, 0x80
	s_cselect_b32 s10, s24, s26
	s_cselect_b32 s11, s25, s27
	s_and_b32 s6, s8, 0x7f
	s_lshl_b32 s6, s6, 10
	s_add_u32 s10, s10, s6
	s_addc_u32 s11, s11, 0
	s_waitcnt lgkmcnt(7)
	v_add_f32_e32 v12, v12, v13
	s_waitcnt lgkmcnt(6)
	v_add_f32_e32 v12, v12, v14
	v_add_f32_e32 v12, v12, v15
	s_waitcnt lgkmcnt(5)
	v_add_f32_e32 v12, v12, v16
	v_add_f32_e32 v12, v12, v17
	s_waitcnt lgkmcnt(4)
	v_add_f32_e32 v12, v12, v18
	v_add_f32_e32 v12, v12, v19
	s_waitcnt lgkmcnt(3)
	v_add_f32_e32 v12, v12, v20
	v_add_f32_e32 v12, v12, v21
	s_waitcnt lgkmcnt(2)
	v_add_f32_e32 v12, v12, v22
	v_add_f32_e32 v12, v12, v23
	s_waitcnt lgkmcnt(1)
	v_add_f32_e32 v12, v12, v24
	v_add_f32_e32 v12, v12, v25
	s_waitcnt lgkmcnt(0)
	v_add_f32_e32 v12, v12, v26
	v_add_f32_e32 v12, v12, v27
	global_store_dword v10, v12, s[10:11]
